# layer-0 w_out and ffn_w13 conversions also deferred (to the layer-0 merge tail); prologue keeps only w_in[0] (224 wq_single tasks)
# speedup vs baseline: 1.0019x; 1.0019x over previous
.LBB0_109:
	v_readlane_b32 s0, v251, 5
	v_readlane_b32 s6, v251, 11
	v_readlane_b32 s7, v251, 12
	s_add_u32 s0, s6, 0x10f00000
	v_writelane_b32 v252, s0, 12
	s_addc_u32 s0, s7, 0
	v_writelane_b32 v252, s0, 13
	s_add_u32 s0, s6, 0x3c90c0
	v_writelane_b32 v252, s0, 14
	s_addc_u32 s0, s7, 0
	v_writelane_b32 v252, s0, 15
	s_add_u32 s0, s6, 0x3ad0c0
	v_writelane_b32 v252, s0, 16
	s_addc_u32 s0, s7, 0
	v_writelane_b32 v252, s0, 17
	s_add_u32 s0, s6, 0x13800000
	v_writelane_b32 v252, s0, 18
	s_addc_u32 s0, s7, 0
	v_writelane_b32 v252, s0, 19
	s_add_u32 s0, s6, 0x33d0c0
	v_writelane_b32 v252, s0, 20
	s_addc_u32 s0, s7, 0
	v_writelane_b32 v252, s0, 21
	s_add_u32 s0, s6, 0x11700000
	v_writelane_b32 v252, s0, 22
	s_addc_u32 s0, s7, 0
	v_writelane_b32 v252, s0, 23
	s_add_u32 s0, s6, 0x3320c0
	v_mov_b32_e32 v0, 0x135f
	v_readlane_b32 s1, v251, 6
	v_writelane_b32 v252, s0, 24
	s_addc_u32 s0, s7, 0
	v_cmp_gt_i32_e32 vcc, s28, v0
	v_readlane_b32 s2, v251, 7
	v_readlane_b32 s3, v251, 8
	v_readlane_b32 s4, v251, 9
	v_readlane_b32 s5, v251, 10
	v_writelane_b32 v252, s0, 25
	s_and_b64 s[0:1], vcc, exec
	s_mov_b64 s[0:1], s[52:53]
	s_mov_b64 s[2:3], s[54:55]
	s_mov_b64 s[4:5], s[56:57]
	s_mov_b64 s[6:7], s[58:59]
	s_mov_b64 s[8:9], s[60:61]
	s_mov_b64 s[10:11], s[62:63]
	s_mov_b64 s[12:13], s[64:65]
	v_writelane_b32 v252, s0, 26
	s_waitcnt lgkmcnt(0)
	s_barrier
	v_writelane_b32 v252, s1, 27
	v_writelane_b32 v252, s2, 28
	v_writelane_b32 v252, s3, 29
	v_writelane_b32 v252, s4, 30
	v_writelane_b32 v252, s5, 31
	v_writelane_b32 v252, s6, 32
	v_writelane_b32 v252, s7, 33
	v_writelane_b32 v252, s8, 34
	v_writelane_b32 v252, s9, 35
	v_writelane_b32 v252, s10, 36
	v_writelane_b32 v252, s11, 37
	v_writelane_b32 v252, s12, 38
	v_writelane_b32 v252, s13, 39
	v_writelane_b32 v252, s14, 40
	v_writelane_b32 v252, s15, 41
	s_cbranch_scc1 .LBB0_253
	s_mov_b32 s98, s28
	v_readlane_b32 s100, v251, 24
	s_movk_i32 s99, 0xe0
	s_mov_b32 s101, 0
	s_mov_b32 s0, 0xfffffc00
	s_cmp_lt_u32 s98, 0x10d0
	s_cselect_b32 s0, 0xfffffc00, s0
	s_cmp_lt_u32 s98, 0xf80
	s_cselect_b32 s0, 0xfffffc00, s0
	s_cmp_lt_u32 s98, 0xda0
	s_cselect_b32 s0, 0xfffffc00, s0
	s_cmp_lt_u32 s98, 0xc60
	s_cselect_b32 s0, 0x700, s0
	s_cmp_lt_u32 s98, 0xc40
	s_cselect_b32 s0, 0x6a0, s0
	s_cmp_lt_u32 s98, 0xc00
	s_cselect_b32 s0, 0x6a0, s0
	s_cmp_lt_u32 s98, 0xb60
	s_cselect_b32 s0, 0xfffff600, s0
	s_cmp_lt_u32 s98, 0xab0
	s_cselect_b32 s0, 0x890, s0
	s_cmp_lt_u32 s98, 0xa90
	s_cselect_b32 s0, 0x770, s0
	s_cmp_lt_u32 s98, 0xa20
	s_cselect_b32 s0, 0x770, s0
	s_cmp_lt_u32 s98, 0x9b0
	s_cselect_b32 s0, 0xfffffeb0, s0
	s_cmp_lt_u32 s98, 0x880
	s_cselect_b32 s0, 0xfffffeb0, s0
	s_cmp_lt_u32 s98, 0x5b0
	s_cselect_b32 s0, 0xfffffeb0, s0
	s_cmp_lt_u32 s98, 0x460
	s_cselect_b32 s0, 0xfffffeb0, s0
	s_cmp_lt_u32 s98, 0x2b0
	s_cselect_b32 s0, 0x1070, s0
	s_cmp_lt_u32 s98, 0x290
	s_cselect_b32 s0, 0xe90, s0
	s_cmp_lt_u32 s98, 0x280
	s_cselect_b32 s0, 0xe90, s0
	s_cmp_lt_u32 s98, 0x1b0
	s_cselect_b32 s0, 0xffffff00, s0
	s_cmp_lt_u32 s98, 0x100
	s_cselect_b32 s0, 0x1200, s0
	s_cmp_lt_u32 s98, 0xe0
	s_cselect_b32 s0, 0xf60, s0
	s_add_i32 s28, s98, s0
	v_lshlrev_b32_e32 v0, 2, v50
	s_add_i32 s0, 0, 0x21000
	v_and_b32_e32 v37, 31, v50
	v_add_u32_e32 v39, s0, v0
	v_cmp_gt_i32_e64 s[0:1], 32, v50
	v_lshlrev_b32_e32 v1, 1, v50
	v_lshlrev_b32_e32 v42, 2, v37
	v_writelane_b32 v252, s0, 42
	v_ashrrev_i32_e32 v40, 3, v50
	v_and_b32_e32 v2, 0xffffffc0, v1
	v_add_u32_e32 v4, 0, v42
	v_writelane_b32 v252, s1, 43
	s_add_i32 s0, 0, 0x21800
	s_movk_i32 s2, 0x84
	v_and_b32_e32 v45, 7, v50
	v_add_u32_e32 v43, s0, v0
	v_add_u32_e32 v82, s0, v42
	v_mad_u64_u32 v[6:7], s[0:1], v2, s2, v[4:5]
	v_mul_lo_u32 v41, v40, s2
	v_lshlrev_b32_e32 v45, 4, v45
	v_add3_u32 v83, v41, v45, 0
	v_lshrrev_b32_e32 v45, 5, v50
	s_movk_i32 s0, 0x2100
	v_and_b32_e32 v35, 28, v0
	v_or_b32_e32 v0, 62, v1
	v_or_b32_e32 v1, 63, v1
	v_mul_lo_u32 v84, v45, s0
	v_mul_lo_u32 v0, v0, s2
	v_mul_lo_u32 v44, v1, s2
	v_or_b32_e32 v10, 2, v2
	v_or_b32_e32 v12, 4, v2
	v_or_b32_e32 v14, 6, v2
	v_or_b32_e32 v16, 8, v2
	v_or_b32_e32 v18, 10, v2
	v_or_b32_e32 v20, 12, v2
	v_or_b32_e32 v22, 14, v2
	v_or_b32_e32 v24, 16, v2
	v_or_b32_e32 v26, 18, v2
	v_or_b32_e32 v28, 20, v2
	v_or_b32_e32 v30, 22, v2
	v_or_b32_e32 v32, 24, v2
	v_or_b32_e32 v34, 26, v2
	v_or_b32_e32 v36, 28, v2
	v_or_b32_e32 v38, 30, v2
	v_ashrrev_i32_e32 v41, 31, v40
	v_or_b32_e32 v42, v84, v42
	v_ashrrev_i32_e32 v3, 31, v2
	v_mov_b32_e32 v8, v2
	v_mov_b32_e32 v1, v2
	v_mov_b32_e32 v5, v10
	v_mov_b32_e32 v7, v12
	v_mov_b32_e32 v9, v14
	v_mov_b32_e32 v11, v16
	v_mov_b32_e32 v13, v18
	v_mov_b32_e32 v15, v20
	v_mov_b32_e32 v17, v22
	v_mov_b32_e32 v19, v24
	v_mov_b32_e32 v21, v26
	v_mov_b32_e32 v23, v28
	v_mov_b32_e32 v25, v30
	v_mov_b32_e32 v27, v32
	v_mov_b32_e32 v29, v34
	v_mov_b32_e32 v31, v36
	v_mov_b32_e32 v33, v38
	v_lshlrev_b64 v[40:41], 2, v[40:41]
	v_add_u32_e32 v42, 0, v42
	v_mov_b32_e32 v45, 0
	v_add_u32_e32 v85, v4, v0
	v_add_u32_e32 v86, v4, v44
	s_branch .LBB0_112
.LBB0_111:
	s_or_b64 exec, exec, s[0:1]
	s_waitcnt lgkmcnt(0)
	s_barrier
	ds_read_b32 v0, v82
	ds_read_b32 v44, v85
	ds_read_b32 v58, v86
	s_mov_b32 s2, 0x42fe0000
	v_add_u32_e32 v57, 0x400, v6
	s_waitcnt lgkmcnt(2)
	v_div_scale_f32 v46, s[0:1], v0, v0, s2
	v_rcp_f32_e32 v47, v46
	v_readlane_b32 s0, v252, 46
	v_readlane_b32 s1, v252, 47
	v_add_u32_e32 v60, 0x800, v6
	v_fma_f32 v48, -v46, v47, 1.0
	v_fmac_f32_e32 v47, v48, v47
	v_div_scale_f32 v48, vcc, s2, v0, s2
	v_mul_f32_e32 v49, v48, v47
	v_fma_f32 v52, -v46, v49, v48
	v_fmac_f32_e32 v49, v52, v47
	v_fma_f32 v46, -v46, v49, v48
	v_div_fmas_f32 v46, v46, v47, v49
	ds_read2_b32 v[48:49], v6 offset1:33
	v_div_fixup_f32 v46, v46, v0, s2
	v_cmp_lt_f32_e32 vcc, 0, v0
	ds_read2_b32 v[52:53], v6 offset0:66 offset1:99
	v_readlane_b32 s28, v252, 44
	v_cndmask_b32_e32 v0, 0, v46, vcc
	s_waitcnt lgkmcnt(1)
	v_mul_f32_e32 v48, v48, v0
	v_rndne_f32_e32 v48, v48
	v_cvt_i32_f32_e32 v54, v48
	v_mul_f32_e32 v48, v0, v49
	v_rndne_f32_e32 v48, v48
	v_cvt_i32_f32_e32 v55, v48
	s_waitcnt lgkmcnt(0)
	v_mul_f32_e32 v48, v0, v52
	v_rndne_f32_e32 v48, v48
	v_cvt_i32_f32_sdwa v52, v48 dst_sel:WORD_1 dst_unused:UNUSED_PAD src0_sel:DWORD
	v_mul_f32_e32 v48, v0, v53
	v_or_b32_e32 v46, s33, v37
	v_rndne_f32_e32 v48, v48
	v_ashrrev_i32_e32 v47, 31, v46
	v_cvt_i32_f32_sdwa v53, v48 dst_sel:BYTE_3 dst_unused:UNUSED_PAD src0_sel:DWORD
	ds_read2_b32 v[48:49], v6 offset0:132 offset1:165
	v_lshlrev_b64 v[46:47], 10, v[46:47]
	v_lshl_add_u64 v[46:47], s[0:1], 0, v[46:47]
	v_lshlrev_b32_e32 v55, 8, v55
	s_mov_b32 s0, 0xc0c0500
	v_perm_b32 v54, v55, v54, s0
	v_and_b32_e32 v52, 0xff0000, v52
	v_or3_b32 v52, v54, v52, v53
	ds_read2_b32 v[54:55], v6 offset0:198 offset1:231
	s_waitcnt lgkmcnt(1)
	v_mul_f32_e32 v48, v0, v48
	v_rndne_f32_e32 v48, v48
	v_cvt_i32_f32_e32 v53, v48
	v_mul_f32_e32 v48, v0, v49
	v_rndne_f32_e32 v48, v48
	v_cvt_i32_f32_e32 v56, v48
	s_waitcnt lgkmcnt(0)
	v_mul_f32_e32 v48, v0, v54
	v_rndne_f32_e32 v48, v48
	v_cvt_i32_f32_sdwa v54, v48 dst_sel:WORD_1 dst_unused:UNUSED_PAD src0_sel:DWORD
	v_mul_f32_e32 v48, v0, v55
	v_rndne_f32_e32 v48, v48
	v_cvt_i32_f32_sdwa v55, v48 dst_sel:BYTE_3 dst_unused:UNUSED_PAD src0_sel:DWORD
	ds_read2_b32 v[48:49], v57 offset0:8 offset1:41
	v_lshlrev_b32_e32 v56, 8, v56
	v_perm_b32 v53, v56, v53, s0
	v_and_b32_e32 v54, 0xff0000, v54
	v_or3_b32 v53, v53, v54, v55
	ds_read2_b32 v[54:55], v57 offset0:74 offset1:107
	s_waitcnt lgkmcnt(1)
	v_mul_f32_e32 v48, v0, v48
	v_rndne_f32_e32 v48, v48
	v_cvt_i32_f32_e32 v56, v48
	v_mul_f32_e32 v48, v0, v49
	v_rndne_f32_e32 v48, v48
	v_cvt_i32_f32_e32 v59, v48
	s_waitcnt lgkmcnt(0)
	v_mul_f32_e32 v48, v0, v54
	v_rndne_f32_e32 v48, v48
	v_cvt_i32_f32_sdwa v54, v48 dst_sel:WORD_1 dst_unused:UNUSED_PAD src0_sel:DWORD
	v_mul_f32_e32 v48, v0, v55
	v_rndne_f32_e32 v48, v48
	v_cvt_i32_f32_sdwa v55, v48 dst_sel:BYTE_3 dst_unused:UNUSED_PAD src0_sel:DWORD
	ds_read2_b32 v[48:49], v57 offset0:140 offset1:173
	v_lshlrev_b32_e32 v59, 8, v59
	v_perm_b32 v56, v59, v56, s0
	v_and_b32_e32 v54, 0xff0000, v54
	v_or3_b32 v54, v56, v54, v55
	ds_read2_b32 v[56:57], v57 offset0:206 offset1:239
	s_waitcnt lgkmcnt(1)
	v_mul_f32_e32 v48, v0, v48
	v_mul_f32_e32 v49, v0, v49
	v_rndne_f32_e32 v48, v48
	v_rndne_f32_e32 v49, v49
	v_cvt_i32_f32_e32 v55, v48
	s_waitcnt lgkmcnt(0)
	v_mul_f32_e32 v48, v0, v56
	v_cvt_i32_f32_e32 v49, v49
	v_rndne_f32_e32 v48, v48
	v_cvt_i32_f32_sdwa v56, v48 dst_sel:WORD_1 dst_unused:UNUSED_PAD src0_sel:DWORD
	v_mul_f32_e32 v48, v0, v57
	v_rndne_f32_e32 v48, v48
	v_cvt_i32_f32_sdwa v57, v48 dst_sel:BYTE_3 dst_unused:UNUSED_PAD src0_sel:DWORD
	v_lshlrev_b32_e32 v59, 8, v49
	ds_read2_b32 v[48:49], v60 offset0:16 offset1:49
	v_perm_b32 v55, v59, v55, s0
	v_and_b32_e32 v56, 0xff0000, v56
	v_lshl_add_u64 v[46:47], v[46:47], 0, v[2:3]
	v_or3_b32 v55, v55, v56, v57
	global_store_dwordx4 v[46:47], v[52:55], off
	ds_read2_b32 v[52:53], v60 offset0:82 offset1:115
	s_waitcnt lgkmcnt(1)
	v_mul_f32_e32 v48, v0, v48
	v_rndne_f32_e32 v48, v48
	v_cvt_i32_f32_e32 v54, v48
	v_mul_f32_e32 v48, v0, v49
	v_rndne_f32_e32 v48, v48
	v_cvt_i32_f32_e32 v55, v48
	s_waitcnt lgkmcnt(0)
	v_mul_f32_e32 v48, v0, v52
	v_rndne_f32_e32 v48, v48
	v_cvt_i32_f32_sdwa v52, v48 dst_sel:WORD_1 dst_unused:UNUSED_PAD src0_sel:DWORD
	v_mul_f32_e32 v48, v0, v53
	v_rndne_f32_e32 v48, v48
	v_cvt_i32_f32_sdwa v53, v48 dst_sel:BYTE_3 dst_unused:UNUSED_PAD src0_sel:DWORD
	ds_read2_b32 v[48:49], v60 offset0:148 offset1:181
	v_lshlrev_b32_e32 v55, 8, v55
	v_perm_b32 v54, v55, v54, s0
	v_and_b32_e32 v52, 0xff0000, v52
	v_or3_b32 v52, v54, v52, v53
	ds_read2_b32 v[54:55], v60 offset0:214 offset1:247
	s_waitcnt lgkmcnt(1)
	v_mul_f32_e32 v48, v0, v48
	v_rndne_f32_e32 v48, v48
	v_cvt_i32_f32_e32 v53, v48
	v_mul_f32_e32 v48, v0, v49
	v_rndne_f32_e32 v48, v48
	v_cvt_i32_f32_e32 v56, v48
	s_waitcnt lgkmcnt(0)
	v_mul_f32_e32 v48, v0, v54
	v_rndne_f32_e32 v48, v48
	v_cvt_i32_f32_sdwa v54, v48 dst_sel:WORD_1 dst_unused:UNUSED_PAD src0_sel:DWORD
	v_mul_f32_e32 v48, v0, v55
	v_rndne_f32_e32 v48, v48
	v_add_u32_e32 v57, 0xc00, v6
	v_cvt_i32_f32_sdwa v55, v48 dst_sel:BYTE_3 dst_unused:UNUSED_PAD src0_sel:DWORD
	ds_read2_b32 v[48:49], v57 offset0:24 offset1:57
	v_lshlrev_b32_e32 v56, 8, v56
	v_perm_b32 v53, v56, v53, s0
	v_and_b32_e32 v54, 0xff0000, v54
	v_or3_b32 v53, v53, v54, v55
	ds_read2_b32 v[54:55], v57 offset0:90 offset1:123
	s_waitcnt lgkmcnt(1)
	v_mul_f32_e32 v48, v0, v48
	v_rndne_f32_e32 v48, v48
	v_cvt_i32_f32_e32 v56, v48
	v_mul_f32_e32 v48, v0, v49
	v_rndne_f32_e32 v48, v48
	v_cvt_i32_f32_e32 v59, v48
	s_waitcnt lgkmcnt(0)
	v_mul_f32_e32 v48, v0, v54
	v_rndne_f32_e32 v48, v48
	v_cvt_i32_f32_sdwa v54, v48 dst_sel:WORD_1 dst_unused:UNUSED_PAD src0_sel:DWORD
	v_mul_f32_e32 v48, v0, v55
	v_rndne_f32_e32 v48, v48
	v_cvt_i32_f32_sdwa v55, v48 dst_sel:BYTE_3 dst_unused:UNUSED_PAD src0_sel:DWORD
	ds_read2_b32 v[48:49], v57 offset0:156 offset1:189
	v_lshlrev_b32_e32 v59, 8, v59
	v_perm_b32 v56, v59, v56, s0
	v_and_b32_e32 v54, 0xff0000, v54
	v_or3_b32 v54, v56, v54, v55
	ds_read2_b32 v[56:57], v57 offset0:222 offset1:255
	s_waitcnt lgkmcnt(1)
	v_mul_f32_e32 v48, v0, v48
	v_mul_f32_e32 v49, v0, v49
	v_rndne_f32_e32 v48, v48
	v_rndne_f32_e32 v49, v49
	v_cvt_i32_f32_e32 v55, v48
	s_waitcnt lgkmcnt(0)
	v_mul_f32_e32 v48, v0, v56
	v_cvt_i32_f32_e32 v49, v49
	v_rndne_f32_e32 v48, v48
	v_cvt_i32_f32_sdwa v56, v48 dst_sel:WORD_1 dst_unused:UNUSED_PAD src0_sel:DWORD
	v_mul_f32_e32 v48, v0, v57
	v_rndne_f32_e32 v48, v48
	v_cvt_i32_f32_sdwa v57, v48 dst_sel:BYTE_3 dst_unused:UNUSED_PAD src0_sel:DWORD
	v_add_u32_e32 v60, 0x1000, v6
	v_lshlrev_b32_e32 v59, 8, v49
	ds_read2_b32 v[48:49], v60 offset0:32 offset1:65
	v_perm_b32 v55, v59, v55, s0
	v_and_b32_e32 v56, 0xff0000, v56
	v_or3_b32 v55, v55, v56, v57
	global_store_dwordx4 v[46:47], v[52:55], off offset:16
	ds_read2_b32 v[52:53], v60 offset0:98 offset1:131
	s_waitcnt lgkmcnt(1)
	v_mul_f32_e32 v48, v0, v48
	v_rndne_f32_e32 v48, v48
	v_cvt_i32_f32_e32 v54, v48
	v_mul_f32_e32 v48, v0, v49
	v_rndne_f32_e32 v48, v48
	v_cvt_i32_f32_e32 v55, v48
	s_waitcnt lgkmcnt(0)
	v_mul_f32_e32 v48, v0, v52
	v_rndne_f32_e32 v48, v48
	v_cvt_i32_f32_sdwa v52, v48 dst_sel:WORD_1 dst_unused:UNUSED_PAD src0_sel:DWORD
	v_mul_f32_e32 v48, v0, v53
	v_rndne_f32_e32 v48, v48
	v_cvt_i32_f32_sdwa v53, v48 dst_sel:BYTE_3 dst_unused:UNUSED_PAD src0_sel:DWORD
	ds_read2_b32 v[48:49], v60 offset0:164 offset1:197
	v_lshlrev_b32_e32 v55, 8, v55
	v_perm_b32 v54, v55, v54, s0
	v_and_b32_e32 v52, 0xff0000, v52
	v_or3_b32 v52, v54, v52, v53
	v_add_u32_e32 v53, 0x1200, v6
	ds_read2_b32 v[54:55], v53 offset0:102 offset1:135
	s_waitcnt lgkmcnt(1)
	v_mul_f32_e32 v48, v0, v48
	v_rndne_f32_e32 v48, v48
	v_cvt_i32_f32_e32 v53, v48
	v_mul_f32_e32 v48, v0, v49
	v_rndne_f32_e32 v48, v48
	v_cvt_i32_f32_e32 v56, v48
	s_waitcnt lgkmcnt(0)
	v_mul_f32_e32 v48, v0, v54
	v_rndne_f32_e32 v48, v48
	v_cvt_i32_f32_sdwa v54, v48 dst_sel:WORD_1 dst_unused:UNUSED_PAD src0_sel:DWORD
	v_mul_f32_e32 v48, v0, v55
	v_rndne_f32_e32 v48, v48
	v_add_u32_e32 v57, 0x1400, v6
	v_cvt_i32_f32_sdwa v55, v48 dst_sel:BYTE_3 dst_unused:UNUSED_PAD src0_sel:DWORD
	ds_read2_b32 v[48:49], v57 offset0:40 offset1:73
	v_lshlrev_b32_e32 v56, 8, v56
	v_perm_b32 v53, v56, v53, s0
	v_and_b32_e32 v54, 0xff0000, v54
	v_or3_b32 v53, v53, v54, v55
	ds_read2_b32 v[54:55], v57 offset0:106 offset1:139
	s_waitcnt lgkmcnt(1)
	v_mul_f32_e32 v48, v0, v48
	v_rndne_f32_e32 v48, v48
	v_cvt_i32_f32_e32 v56, v48
	v_mul_f32_e32 v48, v0, v49
	v_rndne_f32_e32 v48, v48
	v_cvt_i32_f32_e32 v59, v48
	s_waitcnt lgkmcnt(0)
	v_mul_f32_e32 v48, v0, v54
	v_rndne_f32_e32 v48, v48
	v_cvt_i32_f32_sdwa v54, v48 dst_sel:WORD_1 dst_unused:UNUSED_PAD src0_sel:DWORD
	v_mul_f32_e32 v48, v0, v55
	v_rndne_f32_e32 v48, v48
	v_cvt_i32_f32_sdwa v55, v48 dst_sel:BYTE_3 dst_unused:UNUSED_PAD src0_sel:DWORD
	ds_read2_b32 v[48:49], v57 offset0:172 offset1:205
	v_lshlrev_b32_e32 v57, 8, v59
	v_perm_b32 v56, v57, v56, s0
	v_and_b32_e32 v54, 0xff0000, v54
	v_or3_b32 v54, v56, v54, v55
	v_add_u32_e32 v55, 0x1600, v6
	ds_read2_b32 v[56:57], v55 offset0:110 offset1:143
	s_waitcnt lgkmcnt(1)
	v_mul_f32_e32 v48, v0, v48
	v_mul_f32_e32 v49, v0, v49
	v_rndne_f32_e32 v48, v48
	v_rndne_f32_e32 v49, v49
	v_cvt_i32_f32_e32 v55, v48
	s_waitcnt lgkmcnt(0)
	v_mul_f32_e32 v48, v0, v56
	v_cvt_i32_f32_e32 v49, v49
	v_rndne_f32_e32 v48, v48
	v_cvt_i32_f32_sdwa v56, v48 dst_sel:WORD_1 dst_unused:UNUSED_PAD src0_sel:DWORD
	v_mul_f32_e32 v48, v0, v57
	v_rndne_f32_e32 v48, v48
	v_cvt_i32_f32_sdwa v57, v48 dst_sel:BYTE_3 dst_unused:UNUSED_PAD src0_sel:DWORD
	v_add_u32_e32 v60, 0x1800, v6
	v_lshlrev_b32_e32 v59, 8, v49
	ds_read2_b32 v[48:49], v60 offset0:48 offset1:81
	v_perm_b32 v55, v59, v55, s0
	v_and_b32_e32 v56, 0xff0000, v56
	v_or3_b32 v55, v55, v56, v57
	global_store_dwordx4 v[46:47], v[52:55], off offset:32
	ds_read2_b32 v[52:53], v60 offset0:114 offset1:147
	s_waitcnt lgkmcnt(1)
	v_mul_f32_e32 v48, v0, v48
	v_rndne_f32_e32 v48, v48
	v_cvt_i32_f32_e32 v54, v48
	v_mul_f32_e32 v48, v0, v49
	v_rndne_f32_e32 v48, v48
	v_cvt_i32_f32_e32 v55, v48
	s_waitcnt lgkmcnt(0)
	v_mul_f32_e32 v48, v0, v52
	v_rndne_f32_e32 v48, v48
	v_cvt_i32_f32_sdwa v52, v48 dst_sel:WORD_1 dst_unused:UNUSED_PAD src0_sel:DWORD
	v_mul_f32_e32 v48, v0, v53
	v_rndne_f32_e32 v48, v48
	v_cvt_i32_f32_sdwa v53, v48 dst_sel:BYTE_3 dst_unused:UNUSED_PAD src0_sel:DWORD
	ds_read2_b32 v[48:49], v60 offset0:180 offset1:213
	v_lshlrev_b32_e32 v55, 8, v55
	v_perm_b32 v54, v55, v54, s0
	v_and_b32_e32 v52, 0xff0000, v52
	v_or3_b32 v52, v54, v52, v53
	v_add_u32_e32 v53, 0x1a00, v6
	ds_read2_b32 v[54:55], v53 offset0:118 offset1:151
	s_waitcnt lgkmcnt(1)
	v_mul_f32_e32 v48, v0, v48
	v_rndne_f32_e32 v48, v48
	v_cvt_i32_f32_e32 v53, v48
	v_mul_f32_e32 v48, v0, v49
	v_rndne_f32_e32 v48, v48
	v_cvt_i32_f32_e32 v56, v48
	s_waitcnt lgkmcnt(0)
	v_mul_f32_e32 v48, v0, v54
	v_rndne_f32_e32 v48, v48
	v_cvt_i32_f32_sdwa v54, v48 dst_sel:WORD_1 dst_unused:UNUSED_PAD src0_sel:DWORD
	v_mul_f32_e32 v48, v0, v55
	v_rndne_f32_e32 v48, v48
	v_add_u32_e32 v57, 0x1c00, v6
	v_cvt_i32_f32_sdwa v55, v48 dst_sel:BYTE_3 dst_unused:UNUSED_PAD src0_sel:DWORD
	ds_read2_b32 v[48:49], v57 offset0:56 offset1:89
	v_lshlrev_b32_e32 v56, 8, v56
	v_perm_b32 v53, v56, v53, s0
	v_and_b32_e32 v54, 0xff0000, v54
	v_or3_b32 v53, v53, v54, v55
	ds_read2_b32 v[54:55], v57 offset0:122 offset1:155
	s_waitcnt lgkmcnt(1)
	v_mul_f32_e32 v48, v0, v48
	v_rndne_f32_e32 v48, v48
	v_cvt_i32_f32_e32 v56, v48
	v_mul_f32_e32 v48, v0, v49
	v_rndne_f32_e32 v48, v48
	v_cvt_i32_f32_e32 v59, v48
	s_waitcnt lgkmcnt(0)
	v_mul_f32_e32 v48, v0, v54
	v_rndne_f32_e32 v48, v48
	v_cvt_i32_f32_sdwa v54, v48 dst_sel:WORD_1 dst_unused:UNUSED_PAD src0_sel:DWORD
	v_mul_f32_e32 v48, v0, v55
	v_rndne_f32_e32 v48, v48
	v_cvt_i32_f32_sdwa v55, v48 dst_sel:BYTE_3 dst_unused:UNUSED_PAD src0_sel:DWORD
	ds_read2_b32 v[48:49], v57 offset0:188 offset1:221
	v_mul_f32_e32 v44, v0, v44
	v_rndne_f32_e32 v44, v44
	v_cvt_i32_f32_sdwa v44, v44 dst_sel:WORD_1 dst_unused:UNUSED_PAD src0_sel:DWORD
	v_lshlrev_b32_e32 v57, 8, v59
	s_waitcnt lgkmcnt(0)
	v_mul_f32_e32 v49, v0, v49
	v_mul_f32_e32 v48, v0, v48
	v_rndne_f32_e32 v49, v49
	v_rndne_f32_e32 v48, v48
	v_cvt_i32_f32_e32 v49, v49
	v_cvt_i32_f32_e32 v48, v48
	v_mul_f32_e32 v0, v0, v58
	v_rndne_f32_e32 v0, v0
	v_cvt_i32_f32_sdwa v0, v0 dst_sel:BYTE_3 dst_unused:UNUSED_PAD src0_sel:DWORD
	v_lshlrev_b32_e32 v49, 8, v49
	v_perm_b32 v56, v57, v56, s0
	v_perm_b32 v48, v49, v48, s0
	s_add_i32 s98, s98, s100
	v_and_b32_e32 v54, 0xff0000, v54
	v_and_b32_e32 v44, 0xff0000, v44
	s_mov_b32 s0, 0xfffffc00
	s_cmp_lt_u32 s98, 0x10d0
	s_cselect_b32 s0, 0xfffffc00, s0
	s_cmp_lt_u32 s98, 0xf80
	s_cselect_b32 s0, 0xfffffc00, s0
	s_cmp_lt_u32 s98, 0xda0
	s_cselect_b32 s0, 0xfffffc00, s0
	s_cmp_lt_u32 s98, 0xc60
	s_cselect_b32 s0, 0x700, s0
	s_cmp_lt_u32 s98, 0xc40
	s_cselect_b32 s0, 0x6a0, s0
	s_cmp_lt_u32 s98, 0xc00
	s_cselect_b32 s0, 0x6a0, s0
	s_cmp_lt_u32 s98, 0xb60
	s_cselect_b32 s0, 0xfffff600, s0
	s_cmp_lt_u32 s98, 0xab0
	s_cselect_b32 s0, 0x890, s0
	s_cmp_lt_u32 s98, 0xa90
	s_cselect_b32 s0, 0x770, s0
	s_cmp_lt_u32 s98, 0xa20
	s_cselect_b32 s0, 0x770, s0
	s_cmp_lt_u32 s98, 0x9b0
	s_cselect_b32 s0, 0xfffffeb0, s0
	s_cmp_lt_u32 s98, 0x880
	s_cselect_b32 s0, 0xfffffeb0, s0
	s_cmp_lt_u32 s98, 0x5b0
	s_cselect_b32 s0, 0xfffffeb0, s0
	s_cmp_lt_u32 s98, 0x460
	s_cselect_b32 s0, 0xfffffeb0, s0
	s_cmp_lt_u32 s98, 0x2b0
	s_cselect_b32 s0, 0x1070, s0
	s_cmp_lt_u32 s98, 0x290
	s_cselect_b32 s0, 0xe90, s0
	s_cmp_lt_u32 s98, 0x280
	s_cselect_b32 s0, 0xe90, s0
	s_cmp_lt_u32 s98, 0x1b0
	s_cselect_b32 s0, 0xffffff00, s0
	s_cmp_lt_u32 s98, 0x100
	s_cselect_b32 s0, 0x1200, s0
	s_cmp_lt_u32 s98, 0xe0
	s_cselect_b32 s0, 0xf60, s0
	s_add_i32 s28, s98, s0
	v_or3_b32 v54, v56, v54, v55
	v_or3_b32 v55, v48, v44, v0
	s_cmp_ge_u32 s98, s99
	global_store_dwordx4 v[46:47], v[52:55], off offset:48
	s_barrier
	s_cbranch_scc1 .LBB0_253

.LBB0_1028:
	v_readlane_b32 s98, v251, 3
	v_readlane_b32 s99, v255, 29
	s_cmp_lt_u32 s98, 48
	s_cbranch_scc1 .Lwqd_skip_M
	s_sub_i32 s98, s98, 48
	s_mov_b32 s100, 0
	s_mov_b32 s101, 0
	s_cmp_eq_u32 s99, 0
	s_cselect_b32 s100, 0xe0, s100
	s_cselect_b32 s101, 0x280, s101
	s_cmp_eq_u32 s99, 1
	s_cselect_b32 s100, 0x880, s100
	s_cselect_b32 s101, 0xa20, s101
	s_cmp_eq_u32 s99, 2
	s_cselect_b32 s100, 0xc00, s100
	s_cselect_b32 s101, 0xda0, s101
	s_add_i32 s98, s98, s100
	s_mov_b32 s99, s101
	s_cmp_ge_u32 s98, s99
	s_cbranch_scc1 .Lwqd_skip_M
	s_movk_i32 s100, 208
	s_mov_b32 s101, 3
	v_writelane_b32 v117, s0, 0
	v_writelane_b32 v117, s1, 1
	v_writelane_b32 v117, s2, 2
	v_writelane_b32 v117, s3, 3
	v_writelane_b32 v117, s4, 4
	v_writelane_b32 v117, s5, 5
	v_writelane_b32 v117, s6, 6
	v_writelane_b32 v117, s7, 7
	v_writelane_b32 v117, s8, 8
	v_writelane_b32 v117, s9, 9
	v_writelane_b32 v117, s10, 10
	v_writelane_b32 v117, s11, 11
	v_writelane_b32 v117, s12, 12
	v_writelane_b32 v117, s13, 13
	v_writelane_b32 v117, s14, 14
	v_writelane_b32 v117, s15, 15
	v_writelane_b32 v117, s16, 16
	v_writelane_b32 v117, s17, 17
	v_writelane_b32 v117, s18, 18
	v_writelane_b32 v117, s19, 19
	v_writelane_b32 v117, s20, 20
	v_writelane_b32 v117, s21, 21
	v_writelane_b32 v117, s22, 22
	v_writelane_b32 v117, s23, 23
	v_writelane_b32 v117, s24, 24
	v_writelane_b32 v117, s25, 25
	v_writelane_b32 v117, s26, 26
	v_writelane_b32 v117, s27, 27
	v_writelane_b32 v117, s28, 28
	v_writelane_b32 v117, s29, 29
	v_writelane_b32 v117, s30, 30
	v_writelane_b32 v117, s31, 31
	v_writelane_b32 v117, s32, 32
	v_writelane_b32 v117, s33, 33
	v_writelane_b32 v117, s34, 34
	v_writelane_b32 v117, s35, 35
	v_writelane_b32 v117, s36, 36
	v_writelane_b32 v117, s37, 37
	v_writelane_b32 v117, s38, 38
	v_writelane_b32 v117, s39, 39
	v_writelane_b32 v117, s40, 40
	v_writelane_b32 v117, s41, 41
	v_writelane_b32 v117, s42, 42
	v_writelane_b32 v117, s43, 43
	v_writelane_b32 v117, s44, 44
	v_writelane_b32 v117, s45, 45
	v_writelane_b32 v117, s46, 46
	v_writelane_b32 v117, s47, 47
	v_writelane_b32 v117, s48, 48
	v_writelane_b32 v117, s49, 49
	v_writelane_b32 v117, s50, 50
	v_writelane_b32 v117, s51, 51
	v_writelane_b32 v117, s52, 52
	v_writelane_b32 v117, s53, 53
	v_writelane_b32 v117, s54, 54
	v_writelane_b32 v117, s55, 55
	v_writelane_b32 v117, s56, 56
	v_writelane_b32 v117, s57, 57
	v_writelane_b32 v117, s58, 58
	v_writelane_b32 v117, s59, 59
	v_writelane_b32 v117, s60, 60
	v_writelane_b32 v117, s61, 61
	v_writelane_b32 v117, s62, 62
	v_writelane_b32 v117, s63, 63
	v_writelane_b32 v118, s64, 0
	v_writelane_b32 v118, s65, 1
	v_writelane_b32 v118, s66, 2
	v_writelane_b32 v118, s67, 3
	v_writelane_b32 v118, s68, 4
	v_writelane_b32 v118, s69, 5
	v_writelane_b32 v118, s70, 6
	v_writelane_b32 v118, s71, 7
	v_writelane_b32 v118, s72, 8
	v_writelane_b32 v118, s73, 9
	v_writelane_b32 v118, s74, 10
	v_writelane_b32 v118, s75, 11
	v_writelane_b32 v118, s76, 12
	v_writelane_b32 v118, s77, 13
	v_writelane_b32 v118, s78, 14
	v_writelane_b32 v118, s79, 15
	v_writelane_b32 v118, s80, 16
	v_writelane_b32 v118, s81, 17
	v_writelane_b32 v118, s82, 18
	v_writelane_b32 v118, s83, 19
	v_writelane_b32 v118, s84, 20
	v_writelane_b32 v118, s85, 21
	v_writelane_b32 v118, s86, 22
	v_writelane_b32 v118, s87, 23
	v_writelane_b32 v118, s88, 24
	v_writelane_b32 v118, s89, 25
	v_writelane_b32 v118, s90, 26
	v_writelane_b32 v118, s91, 27
	v_writelane_b32 v118, s92, 28
	v_writelane_b32 v118, s93, 29
	v_writelane_b32 v118, s94, 30
	v_writelane_b32 v118, s95, 31
	v_writelane_b32 v118, s96, 32
	v_writelane_b32 v118, s97, 33
	v_mov_b32_e32 v100, v0
	v_mov_b32_e32 v101, v50
	v_mov_b32_e32 v102, v51
	v_mov_b32_e32 v103, v52
	v_mov_b32_e32 v104, v54
	v_mov_b32_e32 v105, v55
	v_mov_b32_e32 v106, v56
	v_mov_b32_e32 v107, v58
	v_mov_b32_e32 v108, v59
	v_mov_b32_e32 v109, v60
	v_mov_b32_e32 v110, v62
	v_mov_b32_e32 v111, v63
	v_mov_b32_e32 v112, v64
	v_mov_b32_e32 v113, v67
	v_mov_b32_e32 v114, v75
	v_mov_b32_e32 v115, v77
	s_branch .Lwqd_entry

.Lwqd_entry:
	v_mov_b32_e32 v50, v246
	v_mov_b32_e32 v5, 0
	v_readlane_b32 s52, v252, 26
	v_readlane_b32 s53, v252, 27
	s_mov_b32 s0, 0xfffffc00
	s_cmp_lt_u32 s98, 0x10d0
	s_cselect_b32 s0, 0xfffffc00, s0
	s_cmp_lt_u32 s98, 0xf80
	s_cselect_b32 s0, 0xfffffc00, s0
	s_cmp_lt_u32 s98, 0xda0
	s_cselect_b32 s0, 0xfffffc00, s0
	s_cmp_lt_u32 s98, 0xc60
	s_cselect_b32 s0, 0x700, s0
	s_cmp_lt_u32 s98, 0xc40
	s_cselect_b32 s0, 0x6a0, s0
	s_cmp_lt_u32 s98, 0xc00
	s_cselect_b32 s0, 0x6a0, s0
	s_cmp_lt_u32 s98, 0xb60
	s_cselect_b32 s0, 0xfffff600, s0
	s_cmp_lt_u32 s98, 0xab0
	s_cselect_b32 s0, 0x890, s0
	s_cmp_lt_u32 s98, 0xa90
	s_cselect_b32 s0, 0x770, s0
	s_cmp_lt_u32 s98, 0xa20
	s_cselect_b32 s0, 0x770, s0
	s_cmp_lt_u32 s98, 0x9b0
	s_cselect_b32 s0, 0xfffffeb0, s0
	s_cmp_lt_u32 s98, 0x880
	s_cselect_b32 s0, 0xfffffeb0, s0
	s_cmp_lt_u32 s98, 0x5b0
	s_cselect_b32 s0, 0xfffffeb0, s0
	s_cmp_lt_u32 s98, 0x460
	s_cselect_b32 s0, 0xfffffeb0, s0
	s_cmp_lt_u32 s98, 0x2b0
	s_cselect_b32 s0, 0x1070, s0
	s_cmp_lt_u32 s98, 0x290
	s_cselect_b32 s0, 0xe90, s0
	s_cmp_lt_u32 s98, 0x280
	s_cselect_b32 s0, 0xe90, s0
	s_cmp_lt_u32 s98, 0x1b0
	s_cselect_b32 s0, 0xffffff00, s0
	s_cmp_lt_u32 s98, 0x100
	s_cselect_b32 s0, 0x1200, s0
	s_cmp_lt_u32 s98, 0xe0
	s_cselect_b32 s0, 0xf60, s0
	s_add_i32 s28, s98, s0
	v_lshlrev_b32_e32 v0, 2, v50
	s_add_i32 s0, 0, 0x21000
	v_and_b32_e32 v37, 31, v50
	v_add_u32_e32 v39, s0, v0
	v_cmp_gt_i32_e64 s[0:1], 32, v50
	v_lshlrev_b32_e32 v1, 1, v50
	v_lshlrev_b32_e32 v42, 2, v37
	v_writelane_b32 v116, s0, 0
	v_ashrrev_i32_e32 v40, 3, v50
	v_and_b32_e32 v2, 0xffffffc0, v1
	v_add_u32_e32 v4, 0, v42
	v_writelane_b32 v116, s1, 1
	s_add_i32 s0, 0, 0x21800
	s_movk_i32 s2, 0x84
	v_and_b32_e32 v45, 7, v50
	v_add_u32_e32 v43, s0, v0
	v_add_u32_e32 v82, s0, v42
	v_mad_u64_u32 v[6:7], s[0:1], v2, s2, v[4:5]
	v_mul_lo_u32 v41, v40, s2
	v_lshlrev_b32_e32 v45, 4, v45
	v_add3_u32 v83, v41, v45, 0
	v_lshrrev_b32_e32 v45, 5, v50
	s_movk_i32 s0, 0x2100
	v_and_b32_e32 v35, 28, v0
	v_or_b32_e32 v0, 62, v1
	v_or_b32_e32 v1, 63, v1
	v_mul_lo_u32 v84, v45, s0
	v_mul_lo_u32 v0, v0, s2
	v_mul_lo_u32 v44, v1, s2
	v_or_b32_e32 v10, 2, v2
	v_or_b32_e32 v12, 4, v2
	v_or_b32_e32 v14, 6, v2
	v_or_b32_e32 v16, 8, v2
	v_or_b32_e32 v18, 10, v2
	v_or_b32_e32 v20, 12, v2
	v_or_b32_e32 v22, 14, v2
	v_or_b32_e32 v24, 16, v2
	v_or_b32_e32 v26, 18, v2
	v_or_b32_e32 v28, 20, v2
	v_or_b32_e32 v30, 22, v2
	v_or_b32_e32 v32, 24, v2
	v_or_b32_e32 v34, 26, v2
	v_or_b32_e32 v36, 28, v2
	v_or_b32_e32 v38, 30, v2
	v_ashrrev_i32_e32 v41, 31, v40
	v_or_b32_e32 v42, v84, v42
	v_ashrrev_i32_e32 v3, 31, v2
	v_mov_b32_e32 v8, v2
	v_mov_b32_e32 v1, v2
	v_mov_b32_e32 v5, v10
	v_mov_b32_e32 v7, v12
	v_mov_b32_e32 v9, v14
	v_mov_b32_e32 v11, v16
	v_mov_b32_e32 v13, v18
	v_mov_b32_e32 v15, v20
	v_mov_b32_e32 v17, v22
	v_mov_b32_e32 v19, v24
	v_mov_b32_e32 v21, v26
	v_mov_b32_e32 v23, v28
	v_mov_b32_e32 v25, v30
	v_mov_b32_e32 v27, v32
	v_mov_b32_e32 v29, v34
	v_mov_b32_e32 v31, v36
	v_mov_b32_e32 v33, v38
	v_lshlrev_b64 v[40:41], 2, v[40:41]
	v_add_u32_e32 v42, 0, v42
	v_mov_b32_e32 v45, 0
	v_add_u32_e32 v85, v4, v0
	v_add_u32_e32 v86, v4, v44
	s_branch .Lwqd_112
.Lwqd_111:
	s_or_b64 exec, exec, s[0:1]
	s_waitcnt lgkmcnt(0)
	s_barrier
	ds_read_b32 v0, v82
	ds_read_b32 v44, v85
	ds_read_b32 v58, v86
	s_mov_b32 s2, 0x42fe0000
	v_add_u32_e32 v57, 0x400, v6
	s_waitcnt lgkmcnt(2)
	v_div_scale_f32 v46, s[0:1], v0, v0, s2
	v_rcp_f32_e32 v47, v46
	v_readlane_b32 s0, v116, 4
	v_readlane_b32 s1, v116, 5
	v_add_u32_e32 v60, 0x800, v6
	v_fma_f32 v48, -v46, v47, 1.0
	v_fmac_f32_e32 v47, v48, v47
	v_div_scale_f32 v48, vcc, s2, v0, s2
	v_mul_f32_e32 v49, v48, v47
	v_fma_f32 v52, -v46, v49, v48
	v_fmac_f32_e32 v49, v52, v47
	v_fma_f32 v46, -v46, v49, v48
	v_div_fmas_f32 v46, v46, v47, v49
	ds_read2_b32 v[48:49], v6 offset1:33
	v_div_fixup_f32 v46, v46, v0, s2
	v_cmp_lt_f32_e32 vcc, 0, v0
	ds_read2_b32 v[52:53], v6 offset0:66 offset1:99
	v_readlane_b32 s28, v116, 2
	v_cndmask_b32_e32 v0, 0, v46, vcc
	s_waitcnt lgkmcnt(1)
	v_mul_f32_e32 v48, v48, v0
	v_rndne_f32_e32 v48, v48
	v_cvt_i32_f32_e32 v54, v48
	v_mul_f32_e32 v48, v0, v49
	v_rndne_f32_e32 v48, v48
	v_cvt_i32_f32_e32 v55, v48
	s_waitcnt lgkmcnt(0)
	v_mul_f32_e32 v48, v0, v52
	v_rndne_f32_e32 v48, v48
	v_cvt_i32_f32_sdwa v52, v48 dst_sel:WORD_1 dst_unused:UNUSED_PAD src0_sel:DWORD
	v_mul_f32_e32 v48, v0, v53
	v_or_b32_e32 v46, s33, v37
	v_rndne_f32_e32 v48, v48
	v_ashrrev_i32_e32 v47, 31, v46
	v_cvt_i32_f32_sdwa v53, v48 dst_sel:BYTE_3 dst_unused:UNUSED_PAD src0_sel:DWORD
	ds_read2_b32 v[48:49], v6 offset0:132 offset1:165
	v_lshlrev_b64 v[46:47], 10, v[46:47]
	v_lshl_add_u64 v[46:47], s[0:1], 0, v[46:47]
	v_lshlrev_b32_e32 v55, 8, v55
	s_mov_b32 s0, 0xc0c0500
	v_perm_b32 v54, v55, v54, s0
	v_and_b32_e32 v52, 0xff0000, v52
	v_or3_b32 v52, v54, v52, v53
	ds_read2_b32 v[54:55], v6 offset0:198 offset1:231
	s_waitcnt lgkmcnt(1)
	v_mul_f32_e32 v48, v0, v48
	v_rndne_f32_e32 v48, v48
	v_cvt_i32_f32_e32 v53, v48
	v_mul_f32_e32 v48, v0, v49
	v_rndne_f32_e32 v48, v48
	v_cvt_i32_f32_e32 v56, v48
	s_waitcnt lgkmcnt(0)
	v_mul_f32_e32 v48, v0, v54
	v_rndne_f32_e32 v48, v48
	v_cvt_i32_f32_sdwa v54, v48 dst_sel:WORD_1 dst_unused:UNUSED_PAD src0_sel:DWORD
	v_mul_f32_e32 v48, v0, v55
	v_rndne_f32_e32 v48, v48
	v_cvt_i32_f32_sdwa v55, v48 dst_sel:BYTE_3 dst_unused:UNUSED_PAD src0_sel:DWORD
	ds_read2_b32 v[48:49], v57 offset0:8 offset1:41
	v_lshlrev_b32_e32 v56, 8, v56
	v_perm_b32 v53, v56, v53, s0
	v_and_b32_e32 v54, 0xff0000, v54
	v_or3_b32 v53, v53, v54, v55
	ds_read2_b32 v[54:55], v57 offset0:74 offset1:107
	s_waitcnt lgkmcnt(1)
	v_mul_f32_e32 v48, v0, v48
	v_rndne_f32_e32 v48, v48
	v_cvt_i32_f32_e32 v56, v48
	v_mul_f32_e32 v48, v0, v49
	v_rndne_f32_e32 v48, v48
	v_cvt_i32_f32_e32 v59, v48
	s_waitcnt lgkmcnt(0)
	v_mul_f32_e32 v48, v0, v54
	v_rndne_f32_e32 v48, v48
	v_cvt_i32_f32_sdwa v54, v48 dst_sel:WORD_1 dst_unused:UNUSED_PAD src0_sel:DWORD
	v_mul_f32_e32 v48, v0, v55
	v_rndne_f32_e32 v48, v48
	v_cvt_i32_f32_sdwa v55, v48 dst_sel:BYTE_3 dst_unused:UNUSED_PAD src0_sel:DWORD
	ds_read2_b32 v[48:49], v57 offset0:140 offset1:173
	v_lshlrev_b32_e32 v59, 8, v59
	v_perm_b32 v56, v59, v56, s0
	v_and_b32_e32 v54, 0xff0000, v54
	v_or3_b32 v54, v56, v54, v55
	ds_read2_b32 v[56:57], v57 offset0:206 offset1:239
	s_waitcnt lgkmcnt(1)
	v_mul_f32_e32 v48, v0, v48
	v_mul_f32_e32 v49, v0, v49
	v_rndne_f32_e32 v48, v48
	v_rndne_f32_e32 v49, v49
	v_cvt_i32_f32_e32 v55, v48
	s_waitcnt lgkmcnt(0)
	v_mul_f32_e32 v48, v0, v56
	v_cvt_i32_f32_e32 v49, v49
	v_rndne_f32_e32 v48, v48
	v_cvt_i32_f32_sdwa v56, v48 dst_sel:WORD_1 dst_unused:UNUSED_PAD src0_sel:DWORD
	v_mul_f32_e32 v48, v0, v57
	v_rndne_f32_e32 v48, v48
	v_cvt_i32_f32_sdwa v57, v48 dst_sel:BYTE_3 dst_unused:UNUSED_PAD src0_sel:DWORD
	v_lshlrev_b32_e32 v59, 8, v49
	ds_read2_b32 v[48:49], v60 offset0:16 offset1:49
	v_perm_b32 v55, v59, v55, s0
	v_and_b32_e32 v56, 0xff0000, v56
	v_lshl_add_u64 v[46:47], v[46:47], 0, v[2:3]
	v_or3_b32 v55, v55, v56, v57
	global_store_dwordx4 v[46:47], v[52:55], off
	ds_read2_b32 v[52:53], v60 offset0:82 offset1:115
	s_waitcnt lgkmcnt(1)
	v_mul_f32_e32 v48, v0, v48
	v_rndne_f32_e32 v48, v48
	v_cvt_i32_f32_e32 v54, v48
	v_mul_f32_e32 v48, v0, v49
	v_rndne_f32_e32 v48, v48
	v_cvt_i32_f32_e32 v55, v48
	s_waitcnt lgkmcnt(0)
	v_mul_f32_e32 v48, v0, v52
	v_rndne_f32_e32 v48, v48
	v_cvt_i32_f32_sdwa v52, v48 dst_sel:WORD_1 dst_unused:UNUSED_PAD src0_sel:DWORD
	v_mul_f32_e32 v48, v0, v53
	v_rndne_f32_e32 v48, v48
	v_cvt_i32_f32_sdwa v53, v48 dst_sel:BYTE_3 dst_unused:UNUSED_PAD src0_sel:DWORD
	ds_read2_b32 v[48:49], v60 offset0:148 offset1:181
	v_lshlrev_b32_e32 v55, 8, v55
	v_perm_b32 v54, v55, v54, s0
	v_and_b32_e32 v52, 0xff0000, v52
	v_or3_b32 v52, v54, v52, v53
	ds_read2_b32 v[54:55], v60 offset0:214 offset1:247
	s_waitcnt lgkmcnt(1)
	v_mul_f32_e32 v48, v0, v48
	v_rndne_f32_e32 v48, v48
	v_cvt_i32_f32_e32 v53, v48
	v_mul_f32_e32 v48, v0, v49
	v_rndne_f32_e32 v48, v48
	v_cvt_i32_f32_e32 v56, v48
	s_waitcnt lgkmcnt(0)
	v_mul_f32_e32 v48, v0, v54
	v_rndne_f32_e32 v48, v48
	v_cvt_i32_f32_sdwa v54, v48 dst_sel:WORD_1 dst_unused:UNUSED_PAD src0_sel:DWORD
	v_mul_f32_e32 v48, v0, v55
	v_rndne_f32_e32 v48, v48
	v_add_u32_e32 v57, 0xc00, v6
	v_cvt_i32_f32_sdwa v55, v48 dst_sel:BYTE_3 dst_unused:UNUSED_PAD src0_sel:DWORD
	ds_read2_b32 v[48:49], v57 offset0:24 offset1:57
	v_lshlrev_b32_e32 v56, 8, v56
	v_perm_b32 v53, v56, v53, s0
	v_and_b32_e32 v54, 0xff0000, v54
	v_or3_b32 v53, v53, v54, v55
	ds_read2_b32 v[54:55], v57 offset0:90 offset1:123
	s_waitcnt lgkmcnt(1)
	v_mul_f32_e32 v48, v0, v48
	v_rndne_f32_e32 v48, v48
	v_cvt_i32_f32_e32 v56, v48
	v_mul_f32_e32 v48, v0, v49
	v_rndne_f32_e32 v48, v48
	v_cvt_i32_f32_e32 v59, v48
	s_waitcnt lgkmcnt(0)
	v_mul_f32_e32 v48, v0, v54
	v_rndne_f32_e32 v48, v48
	v_cvt_i32_f32_sdwa v54, v48 dst_sel:WORD_1 dst_unused:UNUSED_PAD src0_sel:DWORD
	v_mul_f32_e32 v48, v0, v55
	v_rndne_f32_e32 v48, v48
	v_cvt_i32_f32_sdwa v55, v48 dst_sel:BYTE_3 dst_unused:UNUSED_PAD src0_sel:DWORD
	ds_read2_b32 v[48:49], v57 offset0:156 offset1:189
	v_lshlrev_b32_e32 v59, 8, v59
	v_perm_b32 v56, v59, v56, s0
	v_and_b32_e32 v54, 0xff0000, v54
	v_or3_b32 v54, v56, v54, v55
	ds_read2_b32 v[56:57], v57 offset0:222 offset1:255
	s_waitcnt lgkmcnt(1)
	v_mul_f32_e32 v48, v0, v48
	v_mul_f32_e32 v49, v0, v49
	v_rndne_f32_e32 v48, v48
	v_rndne_f32_e32 v49, v49
	v_cvt_i32_f32_e32 v55, v48
	s_waitcnt lgkmcnt(0)
	v_mul_f32_e32 v48, v0, v56
	v_cvt_i32_f32_e32 v49, v49
	v_rndne_f32_e32 v48, v48
	v_cvt_i32_f32_sdwa v56, v48 dst_sel:WORD_1 dst_unused:UNUSED_PAD src0_sel:DWORD
	v_mul_f32_e32 v48, v0, v57
	v_rndne_f32_e32 v48, v48
	v_cvt_i32_f32_sdwa v57, v48 dst_sel:BYTE_3 dst_unused:UNUSED_PAD src0_sel:DWORD
	v_add_u32_e32 v60, 0x1000, v6
	v_lshlrev_b32_e32 v59, 8, v49
	ds_read2_b32 v[48:49], v60 offset0:32 offset1:65
	v_perm_b32 v55, v59, v55, s0
	v_and_b32_e32 v56, 0xff0000, v56
	v_or3_b32 v55, v55, v56, v57
	global_store_dwordx4 v[46:47], v[52:55], off offset:16
	ds_read2_b32 v[52:53], v60 offset0:98 offset1:131
	s_waitcnt lgkmcnt(1)
	v_mul_f32_e32 v48, v0, v48
	v_rndne_f32_e32 v48, v48
	v_cvt_i32_f32_e32 v54, v48
	v_mul_f32_e32 v48, v0, v49
	v_rndne_f32_e32 v48, v48
	v_cvt_i32_f32_e32 v55, v48
	s_waitcnt lgkmcnt(0)
	v_mul_f32_e32 v48, v0, v52
	v_rndne_f32_e32 v48, v48
	v_cvt_i32_f32_sdwa v52, v48 dst_sel:WORD_1 dst_unused:UNUSED_PAD src0_sel:DWORD
	v_mul_f32_e32 v48, v0, v53
	v_rndne_f32_e32 v48, v48
	v_cvt_i32_f32_sdwa v53, v48 dst_sel:BYTE_3 dst_unused:UNUSED_PAD src0_sel:DWORD
	ds_read2_b32 v[48:49], v60 offset0:164 offset1:197
	v_lshlrev_b32_e32 v55, 8, v55
	v_perm_b32 v54, v55, v54, s0
	v_and_b32_e32 v52, 0xff0000, v52
	v_or3_b32 v52, v54, v52, v53
	v_add_u32_e32 v53, 0x1200, v6
	ds_read2_b32 v[54:55], v53 offset0:102 offset1:135
	s_waitcnt lgkmcnt(1)
	v_mul_f32_e32 v48, v0, v48
	v_rndne_f32_e32 v48, v48
	v_cvt_i32_f32_e32 v53, v48
	v_mul_f32_e32 v48, v0, v49
	v_rndne_f32_e32 v48, v48
	v_cvt_i32_f32_e32 v56, v48
	s_waitcnt lgkmcnt(0)
	v_mul_f32_e32 v48, v0, v54
	v_rndne_f32_e32 v48, v48
	v_cvt_i32_f32_sdwa v54, v48 dst_sel:WORD_1 dst_unused:UNUSED_PAD src0_sel:DWORD
	v_mul_f32_e32 v48, v0, v55
	v_rndne_f32_e32 v48, v48
	v_add_u32_e32 v57, 0x1400, v6
	v_cvt_i32_f32_sdwa v55, v48 dst_sel:BYTE_3 dst_unused:UNUSED_PAD src0_sel:DWORD
	ds_read2_b32 v[48:49], v57 offset0:40 offset1:73
	v_lshlrev_b32_e32 v56, 8, v56
	v_perm_b32 v53, v56, v53, s0
	v_and_b32_e32 v54, 0xff0000, v54
	v_or3_b32 v53, v53, v54, v55
	ds_read2_b32 v[54:55], v57 offset0:106 offset1:139
	s_waitcnt lgkmcnt(1)
	v_mul_f32_e32 v48, v0, v48
	v_rndne_f32_e32 v48, v48
	v_cvt_i32_f32_e32 v56, v48
	v_mul_f32_e32 v48, v0, v49
	v_rndne_f32_e32 v48, v48
	v_cvt_i32_f32_e32 v59, v48
	s_waitcnt lgkmcnt(0)
	v_mul_f32_e32 v48, v0, v54
	v_rndne_f32_e32 v48, v48
	v_cvt_i32_f32_sdwa v54, v48 dst_sel:WORD_1 dst_unused:UNUSED_PAD src0_sel:DWORD
	v_mul_f32_e32 v48, v0, v55
	v_rndne_f32_e32 v48, v48
	v_cvt_i32_f32_sdwa v55, v48 dst_sel:BYTE_3 dst_unused:UNUSED_PAD src0_sel:DWORD
	ds_read2_b32 v[48:49], v57 offset0:172 offset1:205
	v_lshlrev_b32_e32 v57, 8, v59
	v_perm_b32 v56, v57, v56, s0
	v_and_b32_e32 v54, 0xff0000, v54
	v_or3_b32 v54, v56, v54, v55
	v_add_u32_e32 v55, 0x1600, v6
	ds_read2_b32 v[56:57], v55 offset0:110 offset1:143
	s_waitcnt lgkmcnt(1)
	v_mul_f32_e32 v48, v0, v48
	v_mul_f32_e32 v49, v0, v49
	v_rndne_f32_e32 v48, v48
	v_rndne_f32_e32 v49, v49
	v_cvt_i32_f32_e32 v55, v48
	s_waitcnt lgkmcnt(0)
	v_mul_f32_e32 v48, v0, v56
	v_cvt_i32_f32_e32 v49, v49
	v_rndne_f32_e32 v48, v48
	v_cvt_i32_f32_sdwa v56, v48 dst_sel:WORD_1 dst_unused:UNUSED_PAD src0_sel:DWORD
	v_mul_f32_e32 v48, v0, v57
	v_rndne_f32_e32 v48, v48
	v_cvt_i32_f32_sdwa v57, v48 dst_sel:BYTE_3 dst_unused:UNUSED_PAD src0_sel:DWORD
	v_add_u32_e32 v60, 0x1800, v6
	v_lshlrev_b32_e32 v59, 8, v49
	ds_read2_b32 v[48:49], v60 offset0:48 offset1:81
	v_perm_b32 v55, v59, v55, s0
	v_and_b32_e32 v56, 0xff0000, v56
	v_or3_b32 v55, v55, v56, v57
	global_store_dwordx4 v[46:47], v[52:55], off offset:32
	ds_read2_b32 v[52:53], v60 offset0:114 offset1:147
	s_waitcnt lgkmcnt(1)
	v_mul_f32_e32 v48, v0, v48
	v_rndne_f32_e32 v48, v48
	v_cvt_i32_f32_e32 v54, v48
	v_mul_f32_e32 v48, v0, v49
	v_rndne_f32_e32 v48, v48
	v_cvt_i32_f32_e32 v55, v48
	s_waitcnt lgkmcnt(0)
	v_mul_f32_e32 v48, v0, v52
	v_rndne_f32_e32 v48, v48
	v_cvt_i32_f32_sdwa v52, v48 dst_sel:WORD_1 dst_unused:UNUSED_PAD src0_sel:DWORD
	v_mul_f32_e32 v48, v0, v53
	v_rndne_f32_e32 v48, v48
	v_cvt_i32_f32_sdwa v53, v48 dst_sel:BYTE_3 dst_unused:UNUSED_PAD src0_sel:DWORD
	ds_read2_b32 v[48:49], v60 offset0:180 offset1:213
	v_lshlrev_b32_e32 v55, 8, v55
	v_perm_b32 v54, v55, v54, s0
	v_and_b32_e32 v52, 0xff0000, v52
	v_or3_b32 v52, v54, v52, v53
	v_add_u32_e32 v53, 0x1a00, v6
	ds_read2_b32 v[54:55], v53 offset0:118 offset1:151
	s_waitcnt lgkmcnt(1)
	v_mul_f32_e32 v48, v0, v48
	v_rndne_f32_e32 v48, v48
	v_cvt_i32_f32_e32 v53, v48
	v_mul_f32_e32 v48, v0, v49
	v_rndne_f32_e32 v48, v48
	v_cvt_i32_f32_e32 v56, v48
	s_waitcnt lgkmcnt(0)
	v_mul_f32_e32 v48, v0, v54
	v_rndne_f32_e32 v48, v48
	v_cvt_i32_f32_sdwa v54, v48 dst_sel:WORD_1 dst_unused:UNUSED_PAD src0_sel:DWORD
	v_mul_f32_e32 v48, v0, v55
	v_rndne_f32_e32 v48, v48
	v_add_u32_e32 v57, 0x1c00, v6
	v_cvt_i32_f32_sdwa v55, v48 dst_sel:BYTE_3 dst_unused:UNUSED_PAD src0_sel:DWORD
	ds_read2_b32 v[48:49], v57 offset0:56 offset1:89
	v_lshlrev_b32_e32 v56, 8, v56
	v_perm_b32 v53, v56, v53, s0
	v_and_b32_e32 v54, 0xff0000, v54
	v_or3_b32 v53, v53, v54, v55
	ds_read2_b32 v[54:55], v57 offset0:122 offset1:155
	s_waitcnt lgkmcnt(1)
	v_mul_f32_e32 v48, v0, v48
	v_rndne_f32_e32 v48, v48
	v_cvt_i32_f32_e32 v56, v48
	v_mul_f32_e32 v48, v0, v49
	v_rndne_f32_e32 v48, v48
	v_cvt_i32_f32_e32 v59, v48
	s_waitcnt lgkmcnt(0)
	v_mul_f32_e32 v48, v0, v54
	v_rndne_f32_e32 v48, v48
	v_cvt_i32_f32_sdwa v54, v48 dst_sel:WORD_1 dst_unused:UNUSED_PAD src0_sel:DWORD
	v_mul_f32_e32 v48, v0, v55
	v_rndne_f32_e32 v48, v48
	v_cvt_i32_f32_sdwa v55, v48 dst_sel:BYTE_3 dst_unused:UNUSED_PAD src0_sel:DWORD
	ds_read2_b32 v[48:49], v57 offset0:188 offset1:221
	v_mul_f32_e32 v44, v0, v44
	v_rndne_f32_e32 v44, v44
	v_cvt_i32_f32_sdwa v44, v44 dst_sel:WORD_1 dst_unused:UNUSED_PAD src0_sel:DWORD
	v_lshlrev_b32_e32 v57, 8, v59
	s_waitcnt lgkmcnt(0)
	v_mul_f32_e32 v49, v0, v49
	v_mul_f32_e32 v48, v0, v48
	v_rndne_f32_e32 v49, v49
	v_rndne_f32_e32 v48, v48
	v_cvt_i32_f32_e32 v49, v49
	v_cvt_i32_f32_e32 v48, v48
	v_mul_f32_e32 v0, v0, v58
	v_rndne_f32_e32 v0, v0
	v_cvt_i32_f32_sdwa v0, v0 dst_sel:BYTE_3 dst_unused:UNUSED_PAD src0_sel:DWORD
	v_lshlrev_b32_e32 v49, 8, v49
	v_perm_b32 v56, v57, v56, s0
	v_perm_b32 v48, v49, v48, s0
	s_add_i32 s98, s98, s100
	v_and_b32_e32 v54, 0xff0000, v54
	v_and_b32_e32 v44, 0xff0000, v44
	s_mov_b32 s0, 0xfffffc00
	s_cmp_lt_u32 s98, 0x10d0
	s_cselect_b32 s0, 0xfffffc00, s0
	s_cmp_lt_u32 s98, 0xf80
	s_cselect_b32 s0, 0xfffffc00, s0
	s_cmp_lt_u32 s98, 0xda0
	s_cselect_b32 s0, 0xfffffc00, s0
	s_cmp_lt_u32 s98, 0xc60
	s_cselect_b32 s0, 0x700, s0
	s_cmp_lt_u32 s98, 0xc40
	s_cselect_b32 s0, 0x6a0, s0
	s_cmp_lt_u32 s98, 0xc00
	s_cselect_b32 s0, 0x6a0, s0
	s_cmp_lt_u32 s98, 0xb60
	s_cselect_b32 s0, 0xfffff600, s0
	s_cmp_lt_u32 s98, 0xab0
	s_cselect_b32 s0, 0x890, s0
	s_cmp_lt_u32 s98, 0xa90
	s_cselect_b32 s0, 0x770, s0
	s_cmp_lt_u32 s98, 0xa20
	s_cselect_b32 s0, 0x770, s0
	s_cmp_lt_u32 s98, 0x9b0
	s_cselect_b32 s0, 0xfffffeb0, s0
	s_cmp_lt_u32 s98, 0x880
	s_cselect_b32 s0, 0xfffffeb0, s0
	s_cmp_lt_u32 s98, 0x5b0
	s_cselect_b32 s0, 0xfffffeb0, s0
	s_cmp_lt_u32 s98, 0x460
	s_cselect_b32 s0, 0xfffffeb0, s0
	s_cmp_lt_u32 s98, 0x2b0
	s_cselect_b32 s0, 0x1070, s0
	s_cmp_lt_u32 s98, 0x290
	s_cselect_b32 s0, 0xe90, s0
	s_cmp_lt_u32 s98, 0x280
	s_cselect_b32 s0, 0xe90, s0
	s_cmp_lt_u32 s98, 0x1b0
	s_cselect_b32 s0, 0xffffff00, s0
	s_cmp_lt_u32 s98, 0x100
	s_cselect_b32 s0, 0x1200, s0
	s_cmp_lt_u32 s98, 0xe0
	s_cselect_b32 s0, 0xf60, s0
	s_add_i32 s28, s98, s0
	v_or3_b32 v54, v56, v54, v55
	v_or3_b32 v55, v48, v44, v0
	s_cmp_ge_u32 s98, s99
	global_store_dwordx4 v[46:47], v[52:55], off offset:48
	s_barrier
	s_cbranch_scc1 .Lwqd_exit

.LBB0_1159:
	v_readlane_b32 s98, v251, 3
	v_readlane_b32 s99, v255, 29
	s_cmp_lt_u32 s98, 16
	s_cbranch_scc1 .Lwqd_skip_A
	s_sub_i32 s98, s98, 16
	s_mov_b32 s100, 0
	s_mov_b32 s101, 0
	s_cmp_eq_u32 s99, 0
	s_cselect_b32 s100, 0x280, s100
	s_cselect_b32 s101, 0x460, s101
	s_cmp_eq_u32 s99, 1
	s_cselect_b32 s100, 0xa20, s100
	s_cselect_b32 s101, 0xc00, s101
	s_cmp_eq_u32 s99, 2
	s_cselect_b32 s100, 0xda0, s100
	s_cselect_b32 s101, 0xf80, s101
	s_add_i32 s98, s98, s100
	s_mov_b32 s99, s101
	s_cmp_ge_u32 s98, s99
	s_cbranch_scc1 .Lwqd_skip_A
	s_movk_i32 s100, 240
	s_mov_b32 s101, 1
	v_writelane_b32 v117, s0, 0
	v_writelane_b32 v117, s1, 1
	v_writelane_b32 v117, s2, 2
	v_writelane_b32 v117, s3, 3
	v_writelane_b32 v117, s4, 4
	v_writelane_b32 v117, s5, 5
	v_writelane_b32 v117, s6, 6
	v_writelane_b32 v117, s7, 7
	v_writelane_b32 v117, s8, 8
	v_writelane_b32 v117, s9, 9
	v_writelane_b32 v117, s10, 10
	v_writelane_b32 v117, s11, 11
	v_writelane_b32 v117, s12, 12
	v_writelane_b32 v117, s13, 13
	v_writelane_b32 v117, s14, 14
	v_writelane_b32 v117, s15, 15
	v_writelane_b32 v117, s16, 16
	v_writelane_b32 v117, s17, 17
	v_writelane_b32 v117, s18, 18
	v_writelane_b32 v117, s19, 19
	v_writelane_b32 v117, s20, 20
	v_writelane_b32 v117, s21, 21
	v_writelane_b32 v117, s22, 22
	v_writelane_b32 v117, s23, 23
	v_writelane_b32 v117, s24, 24
	v_writelane_b32 v117, s25, 25
	v_writelane_b32 v117, s26, 26
	v_writelane_b32 v117, s27, 27
	v_writelane_b32 v117, s28, 28
	v_writelane_b32 v117, s29, 29
	v_writelane_b32 v117, s30, 30
	v_writelane_b32 v117, s31, 31
	v_writelane_b32 v117, s32, 32
	v_writelane_b32 v117, s33, 33
	v_writelane_b32 v117, s34, 34
	v_writelane_b32 v117, s35, 35
	v_writelane_b32 v117, s36, 36
	v_writelane_b32 v117, s37, 37
	v_writelane_b32 v117, s38, 38
	v_writelane_b32 v117, s39, 39
	v_writelane_b32 v117, s40, 40
	v_writelane_b32 v117, s41, 41
	v_writelane_b32 v117, s42, 42
	v_writelane_b32 v117, s43, 43
	v_writelane_b32 v117, s44, 44
	v_writelane_b32 v117, s45, 45
	v_writelane_b32 v117, s46, 46
	v_writelane_b32 v117, s47, 47
	v_writelane_b32 v117, s48, 48
	v_writelane_b32 v117, s49, 49
	v_writelane_b32 v117, s50, 50
	v_writelane_b32 v117, s51, 51
	v_writelane_b32 v117, s52, 52
	v_writelane_b32 v117, s53, 53
	v_writelane_b32 v117, s54, 54
	v_writelane_b32 v117, s55, 55
	v_writelane_b32 v117, s56, 56
	v_writelane_b32 v117, s57, 57
	v_writelane_b32 v117, s58, 58
	v_writelane_b32 v117, s59, 59
	v_writelane_b32 v117, s60, 60
	v_writelane_b32 v117, s61, 61
	v_writelane_b32 v117, s62, 62
	v_writelane_b32 v117, s63, 63
	v_writelane_b32 v118, s64, 0
	v_writelane_b32 v118, s65, 1
	v_writelane_b32 v118, s66, 2
	v_writelane_b32 v118, s67, 3
	v_writelane_b32 v118, s68, 4
	v_writelane_b32 v118, s69, 5
	v_writelane_b32 v118, s70, 6
	v_writelane_b32 v118, s71, 7
	v_writelane_b32 v118, s72, 8
	v_writelane_b32 v118, s73, 9
	v_writelane_b32 v118, s74, 10
	v_writelane_b32 v118, s75, 11
	v_writelane_b32 v118, s76, 12
	v_writelane_b32 v118, s77, 13
	v_writelane_b32 v118, s78, 14
	v_writelane_b32 v118, s79, 15
	v_writelane_b32 v118, s80, 16
	v_writelane_b32 v118, s81, 17
	v_writelane_b32 v118, s82, 18
	v_writelane_b32 v118, s83, 19
	v_writelane_b32 v118, s84, 20
	v_writelane_b32 v118, s85, 21
	v_writelane_b32 v118, s86, 22
	v_writelane_b32 v118, s87, 23
	v_writelane_b32 v118, s88, 24
	v_writelane_b32 v118, s89, 25
	v_writelane_b32 v118, s90, 26
	v_writelane_b32 v118, s91, 27
	v_writelane_b32 v118, s92, 28
	v_writelane_b32 v118, s93, 29
	v_writelane_b32 v118, s94, 30
	v_writelane_b32 v118, s95, 31
	v_writelane_b32 v118, s96, 32
	v_writelane_b32 v118, s97, 33
	v_mov_b32_e32 v100, v0
	v_mov_b32_e32 v101, v50
	v_mov_b32_e32 v102, v51
	v_mov_b32_e32 v103, v52
	v_mov_b32_e32 v104, v54
	v_mov_b32_e32 v105, v55
	v_mov_b32_e32 v106, v56
	v_mov_b32_e32 v107, v58
	v_mov_b32_e32 v108, v59
	v_mov_b32_e32 v109, v60
	v_mov_b32_e32 v110, v62
	v_mov_b32_e32 v111, v63
	v_mov_b32_e32 v112, v64
	v_mov_b32_e32 v113, v67
	v_mov_b32_e32 v114, v75
	v_mov_b32_e32 v115, v77
	s_branch .Lwqd_entry

.LBB0_1699:
	v_readlane_b32 s98, v251, 3
	v_readlane_b32 s99, v255, 29
	s_cmp_lt_u32 s98, 88
	s_cbranch_scc1 .Lwqd_skip_G
	s_sub_i32 s98, s98, 88
	s_mov_b32 s100, 0
	s_mov_b32 s101, 0
	s_cmp_eq_u32 s99, 0
	s_cselect_b32 s100, 0x460, s100
	s_cselect_b32 s101, 0x5b0, s101
	s_cmp_eq_u32 s99, 2
	s_cselect_b32 s100, 0xf80, s100
	s_cselect_b32 s101, 0x10d0, s101
	s_add_i32 s98, s98, s100
	s_mov_b32 s99, s101
	s_cmp_ge_u32 s98, s99
	s_cbranch_scc1 .Lwqd_skip_G
	s_movk_i32 s100, 168
	s_mov_b32 s101, 4
	v_writelane_b32 v117, s0, 0
	v_writelane_b32 v117, s1, 1
	v_writelane_b32 v117, s2, 2
	v_writelane_b32 v117, s3, 3
	v_writelane_b32 v117, s4, 4
	v_writelane_b32 v117, s5, 5
	v_writelane_b32 v117, s6, 6
	v_writelane_b32 v117, s7, 7
	v_writelane_b32 v117, s8, 8
	v_writelane_b32 v117, s9, 9
	v_writelane_b32 v117, s10, 10
	v_writelane_b32 v117, s11, 11
	v_writelane_b32 v117, s12, 12
	v_writelane_b32 v117, s13, 13
	v_writelane_b32 v117, s14, 14
	v_writelane_b32 v117, s15, 15
	v_writelane_b32 v117, s16, 16
	v_writelane_b32 v117, s17, 17
	v_writelane_b32 v117, s18, 18
	v_writelane_b32 v117, s19, 19
	v_writelane_b32 v117, s20, 20
	v_writelane_b32 v117, s21, 21
	v_writelane_b32 v117, s22, 22
	v_writelane_b32 v117, s23, 23
	v_writelane_b32 v117, s24, 24
	v_writelane_b32 v117, s25, 25
	v_writelane_b32 v117, s26, 26
	v_writelane_b32 v117, s27, 27
	v_writelane_b32 v117, s28, 28
	v_writelane_b32 v117, s29, 29
	v_writelane_b32 v117, s30, 30
	v_writelane_b32 v117, s31, 31
	v_writelane_b32 v117, s32, 32
	v_writelane_b32 v117, s33, 33
	v_writelane_b32 v117, s34, 34
	v_writelane_b32 v117, s35, 35
	v_writelane_b32 v117, s36, 36
	v_writelane_b32 v117, s37, 37
	v_writelane_b32 v117, s38, 38
	v_writelane_b32 v117, s39, 39
	v_writelane_b32 v117, s40, 40
	v_writelane_b32 v117, s41, 41
	v_writelane_b32 v117, s42, 42
	v_writelane_b32 v117, s43, 43
	v_writelane_b32 v117, s44, 44
	v_writelane_b32 v117, s45, 45
	v_writelane_b32 v117, s46, 46
	v_writelane_b32 v117, s47, 47
	v_writelane_b32 v117, s48, 48
	v_writelane_b32 v117, s49, 49
	v_writelane_b32 v117, s50, 50
	v_writelane_b32 v117, s51, 51
	v_writelane_b32 v117, s52, 52
	v_writelane_b32 v117, s53, 53
	v_writelane_b32 v117, s54, 54
	v_writelane_b32 v117, s55, 55
	v_writelane_b32 v117, s56, 56
	v_writelane_b32 v117, s57, 57
	v_writelane_b32 v117, s58, 58
	v_writelane_b32 v117, s59, 59
	v_writelane_b32 v117, s60, 60
	v_writelane_b32 v117, s61, 61
	v_writelane_b32 v117, s62, 62
	v_writelane_b32 v117, s63, 63
	v_writelane_b32 v118, s64, 0
	v_writelane_b32 v118, s65, 1
	v_writelane_b32 v118, s66, 2
	v_writelane_b32 v118, s67, 3
	v_writelane_b32 v118, s68, 4
	v_writelane_b32 v118, s69, 5
	v_writelane_b32 v118, s70, 6
	v_writelane_b32 v118, s71, 7
	v_writelane_b32 v118, s72, 8
	v_writelane_b32 v118, s73, 9
	v_writelane_b32 v118, s74, 10
	v_writelane_b32 v118, s75, 11
	v_writelane_b32 v118, s76, 12
	v_writelane_b32 v118, s77, 13
	v_writelane_b32 v118, s78, 14
	v_writelane_b32 v118, s79, 15
	v_writelane_b32 v118, s80, 16
	v_writelane_b32 v118, s81, 17
	v_writelane_b32 v118, s82, 18
	v_writelane_b32 v118, s83, 19
	v_writelane_b32 v118, s84, 20
	v_writelane_b32 v118, s85, 21
	v_writelane_b32 v118, s86, 22
	v_writelane_b32 v118, s87, 23
	v_writelane_b32 v118, s88, 24
	v_writelane_b32 v118, s89, 25
	v_writelane_b32 v118, s90, 26
	v_writelane_b32 v118, s91, 27
	v_writelane_b32 v118, s92, 28
	v_writelane_b32 v118, s93, 29
	v_writelane_b32 v118, s94, 30
	v_writelane_b32 v118, s95, 31
	v_writelane_b32 v118, s96, 32
	v_writelane_b32 v118, s97, 33
	v_mov_b32_e32 v100, v0
	v_mov_b32_e32 v101, v50
	v_mov_b32_e32 v102, v51
	v_mov_b32_e32 v103, v52
	v_mov_b32_e32 v104, v54
	v_mov_b32_e32 v105, v55
	v_mov_b32_e32 v106, v56
	v_mov_b32_e32 v107, v58
	v_mov_b32_e32 v108, v59
	v_mov_b32_e32 v109, v60
	v_mov_b32_e32 v110, v62
	v_mov_b32_e32 v111, v63
	v_mov_b32_e32 v112, v64
	v_mov_b32_e32 v113, v67
	v_mov_b32_e32 v114, v75
	v_mov_b32_e32 v115, v77
	s_branch .Lwqd_entry

.LBB0_1774:
	v_readlane_b32 s98, v251, 3
	v_readlane_b32 s99, v255, 29
	s_cmp_lt_u32 s98, 16
	s_cbranch_scc1 .Lwqd_skip_F
	s_sub_i32 s98, s98, 16
	s_mov_b32 s100, 0
	s_mov_b32 s101, 0
	s_cmp_eq_u32 s99, 0
	s_cselect_b32 s100, 0x5b0, s100
	s_cselect_b32 s101, 0x880, s101
	s_cmp_eq_u32 s99, 2
	s_cselect_b32 s100, 0x10d0, s100
	s_cselect_b32 s101, 0x1360, s101
	s_add_i32 s98, s98, s100
	s_mov_b32 s99, s101
	s_cmp_ge_u32 s98, s99
	s_cbranch_scc1 .Lwqd_skip_F
	s_movk_i32 s100, 240
	s_mov_b32 s101, 2
	v_writelane_b32 v117, s0, 0
	v_writelane_b32 v117, s1, 1
	v_writelane_b32 v117, s2, 2
	v_writelane_b32 v117, s3, 3
	v_writelane_b32 v117, s4, 4
	v_writelane_b32 v117, s5, 5
	v_writelane_b32 v117, s6, 6
	v_writelane_b32 v117, s7, 7
	v_writelane_b32 v117, s8, 8
	v_writelane_b32 v117, s9, 9
	v_writelane_b32 v117, s10, 10
	v_writelane_b32 v117, s11, 11
	v_writelane_b32 v117, s12, 12
	v_writelane_b32 v117, s13, 13
	v_writelane_b32 v117, s14, 14
	v_writelane_b32 v117, s15, 15
	v_writelane_b32 v117, s16, 16
	v_writelane_b32 v117, s17, 17
	v_writelane_b32 v117, s18, 18
	v_writelane_b32 v117, s19, 19
	v_writelane_b32 v117, s20, 20
	v_writelane_b32 v117, s21, 21
	v_writelane_b32 v117, s22, 22
	v_writelane_b32 v117, s23, 23
	v_writelane_b32 v117, s24, 24
	v_writelane_b32 v117, s25, 25
	v_writelane_b32 v117, s26, 26
	v_writelane_b32 v117, s27, 27
	v_writelane_b32 v117, s28, 28
	v_writelane_b32 v117, s29, 29
	v_writelane_b32 v117, s30, 30
	v_writelane_b32 v117, s31, 31
	v_writelane_b32 v117, s32, 32
	v_writelane_b32 v117, s33, 33
	v_writelane_b32 v117, s34, 34
	v_writelane_b32 v117, s35, 35
	v_writelane_b32 v117, s36, 36
	v_writelane_b32 v117, s37, 37
	v_writelane_b32 v117, s38, 38
	v_writelane_b32 v117, s39, 39
	v_writelane_b32 v117, s40, 40
	v_writelane_b32 v117, s41, 41
	v_writelane_b32 v117, s42, 42
	v_writelane_b32 v117, s43, 43
	v_writelane_b32 v117, s44, 44
	v_writelane_b32 v117, s45, 45
	v_writelane_b32 v117, s46, 46
	v_writelane_b32 v117, s47, 47
	v_writelane_b32 v117, s48, 48
	v_writelane_b32 v117, s49, 49
	v_writelane_b32 v117, s50, 50
	v_writelane_b32 v117, s51, 51
	v_writelane_b32 v117, s52, 52
	v_writelane_b32 v117, s53, 53
	v_writelane_b32 v117, s54, 54
	v_writelane_b32 v117, s55, 55
	v_writelane_b32 v117, s56, 56
	v_writelane_b32 v117, s57, 57
	v_writelane_b32 v117, s58, 58
	v_writelane_b32 v117, s59, 59
	v_writelane_b32 v117, s60, 60
	v_writelane_b32 v117, s61, 61
	v_writelane_b32 v117, s62, 62
	v_writelane_b32 v117, s63, 63
	v_writelane_b32 v118, s64, 0
	v_writelane_b32 v118, s65, 1
	v_writelane_b32 v118, s66, 2
	v_writelane_b32 v118, s67, 3
	v_writelane_b32 v118, s68, 4
	v_writelane_b32 v118, s69, 5
	v_writelane_b32 v118, s70, 6
	v_writelane_b32 v118, s71, 7
	v_writelane_b32 v118, s72, 8
	v_writelane_b32 v118, s73, 9
	v_writelane_b32 v118, s74, 10
	v_writelane_b32 v118, s75, 11
	v_writelane_b32 v118, s76, 12
	v_writelane_b32 v118, s77, 13
	v_writelane_b32 v118, s78, 14
	v_writelane_b32 v118, s79, 15
	v_writelane_b32 v118, s80, 16
	v_writelane_b32 v118, s81, 17
	v_writelane_b32 v118, s82, 18
	v_writelane_b32 v118, s83, 19
	v_writelane_b32 v118, s84, 20
	v_writelane_b32 v118, s85, 21
	v_writelane_b32 v118, s86, 22
	v_writelane_b32 v118, s87, 23
	v_writelane_b32 v118, s88, 24
	v_writelane_b32 v118, s89, 25
	v_writelane_b32 v118, s90, 26
	v_writelane_b32 v118, s91, 27
	v_writelane_b32 v118, s92, 28
	v_writelane_b32 v118, s93, 29
	v_writelane_b32 v118, s94, 30
	v_writelane_b32 v118, s95, 31
	v_writelane_b32 v118, s96, 32
	v_writelane_b32 v118, s97, 33
	v_mov_b32_e32 v100, v0
	v_mov_b32_e32 v101, v50
	v_mov_b32_e32 v102, v51
	v_mov_b32_e32 v103, v52
	v_mov_b32_e32 v104, v54
	v_mov_b32_e32 v105, v55
	v_mov_b32_e32 v106, v56
	v_mov_b32_e32 v107, v58
	v_mov_b32_e32 v108, v59
	v_mov_b32_e32 v109, v60
	v_mov_b32_e32 v110, v62
	v_mov_b32_e32 v111, v63
	v_mov_b32_e32 v112, v64
	v_mov_b32_e32 v113, v67
	v_mov_b32_e32 v114, v75
	v_mov_b32_e32 v115, v77
	s_branch .Lwqd_entry
